# mixout gate mat-vec [16x64]x[64x256] moved from packed-f32 VALU to f32-operand MFMA (v_mfma_f32_16x16x4_f32), results redistributed through LDS
# speedup vs baseline: 1.0137x; 1.0137x over previous
.LBB0_1234:
	v_and_b32_e32 v230, 15, v203
	v_lshrrev_b32_e32 v224, 4, v203
	v_lshlrev_b32_e32 v2, 8, v230
	v_lshl_add_u32 v2, v224, 6, v2
	ds_read_b128 v[194:197], v2
	ds_read_b128 v[204:207], v2 offset:16
	ds_read_b128 v[226:229], v2 offset:32
	ds_read_b128 v[68:71], v2 offset:48
	v_readfirstlane_b32 s0, v0
	v_lshlrev_b32_e32 v3, 14, v224
	s_lshr_b32 s0, s0, 6
	s_lshl_b32 s0, s0, 7
	v_lshl_add_u32 v230, v230, 3, v3
	v_add_u32_e32 v230, s0, v230
	v_add_u32_e32 v230, 0x2000, v230
	ds_read_b64 v[54:55], v230 offset:0
	ds_read_b64 v[60:61], v230 offset:1024
	ds_read_b64 v[198:199], v230 offset:2048
	ds_read_b64 v[208:209], v230 offset:3072
	s_waitcnt lgkmcnt(0)
	v_mfma_f32_16x16x4_f32 v[64:67], v194, v54, 0
	v_mfma_f32_16x16x4_f32 v[2:5], v194, v55, 0
	v_mfma_f32_16x16x4_f32 v[64:67], v195, v60, v[64:67]
	v_mfma_f32_16x16x4_f32 v[2:5], v195, v61, v[2:5]
	v_mfma_f32_16x16x4_f32 v[64:67], v196, v198, v[64:67]
	v_mfma_f32_16x16x4_f32 v[2:5], v196, v199, v[2:5]
	v_mfma_f32_16x16x4_f32 v[64:67], v197, v208, v[64:67]
	v_mfma_f32_16x16x4_f32 v[2:5], v197, v209, v[2:5]
	s_nop 7
	ds_read_b64 v[54:55], v230 offset:4096
	ds_read_b64 v[60:61], v230 offset:5120
	ds_read_b64 v[198:199], v230 offset:6144
	ds_read_b64 v[208:209], v230 offset:7168
	s_waitcnt lgkmcnt(0)
	v_mfma_f32_16x16x4_f32 v[64:67], v204, v54, v[64:67]
	v_mfma_f32_16x16x4_f32 v[2:5], v204, v55, v[2:5]
	v_mfma_f32_16x16x4_f32 v[64:67], v205, v60, v[64:67]
	v_mfma_f32_16x16x4_f32 v[2:5], v205, v61, v[2:5]
	v_mfma_f32_16x16x4_f32 v[64:67], v206, v198, v[64:67]
	v_mfma_f32_16x16x4_f32 v[2:5], v206, v199, v[2:5]
	v_mfma_f32_16x16x4_f32 v[64:67], v207, v208, v[64:67]
	v_mfma_f32_16x16x4_f32 v[2:5], v207, v209, v[2:5]
	s_nop 7
	ds_read_b64 v[54:55], v230 offset:8192
	ds_read_b64 v[60:61], v230 offset:9216
	ds_read_b64 v[198:199], v230 offset:10240
	ds_read_b64 v[208:209], v230 offset:11264
	s_waitcnt lgkmcnt(0)
	v_mfma_f32_16x16x4_f32 v[64:67], v226, v54, v[64:67]
	v_mfma_f32_16x16x4_f32 v[2:5], v226, v55, v[2:5]
	v_mfma_f32_16x16x4_f32 v[64:67], v227, v60, v[64:67]
	v_mfma_f32_16x16x4_f32 v[2:5], v227, v61, v[2:5]
	v_mfma_f32_16x16x4_f32 v[64:67], v228, v198, v[64:67]
	v_mfma_f32_16x16x4_f32 v[2:5], v228, v199, v[2:5]
	v_mfma_f32_16x16x4_f32 v[64:67], v229, v208, v[64:67]
	v_mfma_f32_16x16x4_f32 v[2:5], v229, v209, v[2:5]
	s_nop 7
	ds_read_b64 v[54:55], v230 offset:12288
	ds_read_b64 v[60:61], v230 offset:13312
	ds_read_b64 v[198:199], v230 offset:14336
	ds_read_b64 v[208:209], v230 offset:15360
	s_waitcnt lgkmcnt(0)
	v_mfma_f32_16x16x4_f32 v[64:67], v68, v54, v[64:67]
	v_mfma_f32_16x16x4_f32 v[2:5], v68, v55, v[2:5]
	v_mfma_f32_16x16x4_f32 v[64:67], v69, v60, v[64:67]
	v_mfma_f32_16x16x4_f32 v[2:5], v69, v61, v[2:5]
	v_mfma_f32_16x16x4_f32 v[64:67], v70, v198, v[64:67]
	v_mfma_f32_16x16x4_f32 v[2:5], v70, v199, v[2:5]
	v_mfma_f32_16x16x4_f32 v[64:67], v71, v208, v[64:67]
	v_mfma_f32_16x16x4_f32 v[2:5], v71, v209, v[2:5]
	s_nop 7
	v_and_b32_e32 v230, 15, v203
	v_lshrrev_b32_e32 v224, 4, v203
	v_lshlrev_b32_e32 v224, 4, v224
	v_lshl_add_u32 v224, v230, 7, v224
	s_lshl_b32 s0, s0, 4
	v_add_u32_e32 v224, s0, v224
	v_add_u32_e32 v224, 0x14000, v224
	s_nop 15
	s_nop 15
	ds_write_b128 v224, v[64:67]
	ds_write_b128 v224, v[2:5] offset:64
	v_and_b32_e32 v230, 0xff, v0
	v_lshrrev_b32_e32 v198, 8, v0
	v_lshlrev_b32_e32 v230, 6, v230
	v_lshl_add_u32 v230, v198, 5, v230
	v_add_u32_e32 v230, 0x14000, v230
	s_waitcnt lgkmcnt(0)
	s_barrier
	ds_read_b64 v[66:67], v230
	ds_read_b64 v[64:65], v230 offset:8
	ds_read_b64 v[60:61], v230 offset:16
	ds_read_b64 v[54:55], v230 offset:24
	s_movk_i32 s0, 0x100
	s_waitcnt lgkmcnt(0)
	v_lshlrev_b32_e32 v196, 16, v170
	v_lshlrev_b32_e32 v237, 16, v172
	v_lshlrev_b32_e32 v236, 16, v173
	v_lshlrev_b32_e32 v233, 16, v176
	global_load_dword v176, v[20:21], off
	global_load_dword v173, v[22:23], off
	global_load_dword v170, v[24:25], off
	global_load_dword v172, v[26:27], off
	v_and_b32_e32 v2, 64, v203
	v_add_u32_e32 v69, 64, v2
	v_xor_b32_e32 v2, 1, v203
	v_cmp_lt_i32_e64 s[2:3], v2, v69
	v_xor_b32_e32 v3, 2, v203
	v_xor_b32_e32 v4, 4, v203
	v_cndmask_b32_e64 v2, v203, v2, s[2:3]
	v_cmp_lt_i32_e64 s[2:3], v3, v69
	v_xor_b32_e32 v5, 8, v203
	v_xor_b32_e32 v68, 16, v203
	v_cndmask_b32_e64 v3, v203, v3, s[2:3]
	v_cmp_lt_i32_e64 s[2:3], v4, v69
	v_lshlrev_b32_e32 v194, 16, v163
	v_lshlrev_b32_e32 v224, 16, v191
	v_cndmask_b32_e64 v4, v203, v4, s[2:3]
	v_cmp_lt_i32_e64 s[2:3], v5, v69
	v_lshlrev_b32_e32 v191, 16, v192
	v_xor_b32_e32 v192, 32, v203
	v_cndmask_b32_e64 v5, v203, v5, s[2:3]
	v_cmp_lt_i32_e64 s[2:3], v68, v69
	v_lshlrev_b32_e32 v183, 16, v183
	v_add_f32_e32 v183, v183, v194
	v_cndmask_b32_e64 v68, v203, v68, s[2:3]
	v_cmp_lt_i32_e64 s[2:3], v192, v69
	v_lshlrev_b32_e32 v2, 2, v2
	v_lshlrev_b32_e32 v3, 2, v3
	v_cndmask_b32_e64 v69, v203, v192, s[2:3]
	v_mul_f32_e32 v192, v183, v183
	s_nop 1
	v_mov_b32_dpp v192, v192 quad_perm:[1,0,3,2] row_mask:0xf bank_mask:0xf
	v_lshlrev_b32_e32 v225, 16, v190
	v_lshlrev_b32_e32 v190, 16, v193
	v_lshlrev_b32_e32 v4, 2, v4
	v_lshlrev_b32_e32 v5, 2, v5
	s_waitcnt lgkmcnt(0)
	v_fmac_f32_e32 v192, v183, v183
	s_nop 1
	v_mov_b32_dpp v193, v192 quad_perm:[2,3,0,1] row_mask:0xf bank_mask:0xf
	v_lshlrev_b32_e32 v68, 2, v68
	v_lshlrev_b32_e32 v69, 2, v69
	v_lshlrev_b32_e32 v184, 16, v184
	v_lshlrev_b32_e32 v195, 16, v169
	s_waitcnt lgkmcnt(0)
	v_add_f32_e32 v192, v192, v193
	s_nop 1
	v_mov_b32_dpp v193, v192 row_half_mirror row_mask:0xf bank_mask:0xf
	v_lshlrev_b32_e32 v181, 16, v181
	v_add_f32_e32 v181, v181, v195
	v_lshlrev_b32_e32 v179, 16, v179
	v_mul_f32_e32 v179, v196, v179
	s_waitcnt lgkmcnt(0)
	v_add_f32_e32 v192, v192, v193
	s_nop 1
	v_mov_b32_dpp v193, v192 row_mirror row_mask:0xf bank_mask:0xf
	v_lshlrev_b32_e32 v238, 16, v171
	v_lshlrev_b64 v[62:63], 11, v[62:63]
	v_lshl_add_u64 v[62:63], v[28:29], 0, v[62:63]
	v_lshlrev_b32_e32 v235, 16, v174
	s_waitcnt lgkmcnt(0)
	v_add_f32_e32 v192, v192, v193
	v_mov_b32_e32 v193, v192
	s_nop 1
	v_permlane16_swap_b32_e32 v193, v192
	v_lshlrev_b32_e32 v234, 16, v175
	v_lshlrev_b64 v[58:59], 11, v[58:59]
	v_lshl_add_u64 v[58:59], v[28:29], 0, v[58:59]
	v_lshlrev_b32_e32 v232, 16, v180
	s_waitcnt lgkmcnt(0)
	v_add_f32_e32 v192, v192, v193
	v_mov_b32_e32 v193, v192
	s_nop 1
	v_permlane32_swap_b32_e32 v193, v192
	v_lshlrev_b32_e32 v231, 16, v182
	v_lshlrev_b32_e32 v230, 16, v185
	v_lshlrev_b64 v[56:57], 11, v[56:57]
	v_lshl_add_u64 v[56:57], v[28:29], 0, v[56:57]
	s_waitcnt lgkmcnt(0)
	v_add_f32_e32 v192, v192, v193
	v_fmamk_f32 v192, v192, 0x3c800000, v165
	v_rsq_f32_e32 v192, v192
	v_lshlrev_b32_e32 v229, 16, v186
	v_lshlrev_b32_e32 v228, 16, v187
	v_lshlrev_b32_e32 v227, 16, v188
	v_mul_f32_e32 v183, v183, v192
	v_mul_f32_e32 v192, 0xbfb8aa3b, v184
	v_exp_f32_e32 v192, v192
	v_lshlrev_b32_e32 v226, 16, v189
	v_lshlrev_b64 v[52:53], 11, v[52:53]
	v_lshl_add_u64 v[52:53], v[28:29], 0, v[52:53]
	v_add_f32_e32 v192, 1.0, v192
	v_rcp_f32_e32 v192, v192
	s_waitcnt vmcnt(3)
	v_mul_f32_e32 v183, v176, v183
	v_lshlrev_b64 v[50:51], 11, v[50:51]
	v_lshl_add_u64 v[50:51], v[28:29], 0, v[50:51]
	v_mul_f32_e32 v184, v192, v184
	v_mul_f32_e32 v183, v184, v183
	s_nop 1
	v_mov_b32_dpp v184, v181 quad_perm:[1,0,3,2] row_mask:0xf bank_mask:0xf
	v_lshlrev_b32_e32 v189, 16, v210
	v_lshlrev_b32_e32 v188, 16, v211
	v_lshlrev_b32_e32 v187, 16, v212
	v_lshlrev_b32_e32 v186, 16, v213
	s_waitcnt lgkmcnt(0)
	v_add_f32_e32 v184, v181, v184
	s_nop 1
	v_mov_b32_dpp v192, v184 quad_perm:[2,3,0,1] row_mask:0xf bank_mask:0xf
	v_lshlrev_b64 v[48:49], 11, v[48:49]
	v_lshl_add_u64 v[48:49], v[28:29], 0, v[48:49]
	v_lshlrev_b32_e32 v185, 16, v214
	v_lshlrev_b32_e32 v182, 16, v215
	s_waitcnt lgkmcnt(0)
	v_add_f32_e32 v184, v184, v192
	s_nop 1
	v_mov_b32_dpp v192, v184 row_half_mirror row_mask:0xf bank_mask:0xf
	v_lshlrev_b32_e32 v180, 16, v216
	v_lshlrev_b32_e32 v175, 16, v217
	v_lshlrev_b64 v[46:47], 11, v[46:47]
	v_lshl_add_u64 v[46:47], v[28:29], 0, v[46:47]
	s_waitcnt lgkmcnt(0)
	v_add_f32_e32 v184, v184, v192
	s_nop 1
	v_mov_b32_dpp v192, v184 row_mirror row_mask:0xf bank_mask:0xf
	v_lshlrev_b32_e32 v174, 16, v218
	v_lshlrev_b32_e32 v171, 16, v219
	v_lshlrev_b32_e32 v169, 16, v220
	v_lshlrev_b32_e32 v163, 16, v221
	s_waitcnt lgkmcnt(0)
	v_add_f32_e32 v184, v184, v192
	v_mov_b32_e32 v192, v184
	s_nop 1
	v_permlane16_swap_b32_e32 v192, v184
	v_lshlrev_b64 v[44:45], 11, v[44:45]
	v_lshl_add_u64 v[44:45], v[28:29], 0, v[44:45]
	v_lshlrev_b32_e32 v71, 16, v222
	v_lshlrev_b32_e32 v70, 16, v223
	s_waitcnt lgkmcnt(0)
	v_add_f32_e32 v184, v184, v192
	v_mov_b32_e32 v192, v184
	s_nop 1
	v_permlane32_swap_b32_e32 v192, v184
	s_waitcnt lgkmcnt(0)
	v_add_f32_e32 v184, v184, v192
	v_fmac_f32_e32 v181, 0xbc800000, v184
	v_mul_f32_e32 v184, v181, v181
	s_nop 1
	v_mov_b32_dpp v184, v184 quad_perm:[1,0,3,2] row_mask:0xf bank_mask:0xf
	s_waitcnt lgkmcnt(0)
	v_fmac_f32_e32 v184, v181, v181
	s_nop 1
	v_mov_b32_dpp v192, v184 quad_perm:[2,3,0,1] row_mask:0xf bank_mask:0xf
	s_waitcnt lgkmcnt(0)
	v_add_f32_e32 v184, v184, v192
	s_nop 1
	v_mov_b32_dpp v192, v184 row_half_mirror row_mask:0xf bank_mask:0xf
	s_waitcnt lgkmcnt(0)
	v_add_f32_e32 v184, v184, v192
	s_nop 1
	v_mov_b32_dpp v192, v184 row_mirror row_mask:0xf bank_mask:0xf
	s_waitcnt lgkmcnt(0)
	v_add_f32_e32 v184, v184, v192
	v_mov_b32_e32 v192, v184
	s_nop 1
	v_permlane16_swap_b32_e32 v192, v184
	s_waitcnt lgkmcnt(0)
	v_add_f32_e32 v184, v184, v192
	v_mov_b32_e32 v192, v184
	s_nop 1
	v_permlane32_swap_b32_e32 v192, v184
	s_waitcnt lgkmcnt(0)
	v_add_f32_e32 v184, v184, v192
	v_fmamk_f32 v184, v184, 0x3c800000, v164
	v_rsq_f32_e32 v184, v184
	s_nop 0
	v_mul_f32_e32 v181, v181, v184
	s_waitcnt vmcnt(0)
	v_mul_f32_e32 v184, v179, v172
	s_nop 1
	v_mov_b32_dpp v184, v184 quad_perm:[1,0,3,2] row_mask:0xf bank_mask:0xf
	v_fma_f32 v181, v173, v181, v170
	s_waitcnt lgkmcnt(0)
	v_fmac_f32_e32 v184, v179, v172
	s_nop 1
	v_mov_b32_dpp v179, v184 quad_perm:[2,3,0,1] row_mask:0xf bank_mask:0xf
	s_waitcnt lgkmcnt(0)
	v_add_f32_e32 v179, v184, v179
	s_nop 1
	v_mov_b32_dpp v184, v179 row_half_mirror row_mask:0xf bank_mask:0xf
	s_waitcnt lgkmcnt(0)
	v_add_f32_e32 v179, v179, v184
	s_nop 1
	v_mov_b32_dpp v184, v179 row_mirror row_mask:0xf bank_mask:0xf
	s_waitcnt lgkmcnt(0)
	v_add_f32_e32 v179, v179, v184
	v_mov_b32_e32 v184, v179
	s_nop 1
	v_permlane16_swap_b32_e32 v184, v179
	s_waitcnt lgkmcnt(0)
	v_add_f32_e32 v179, v179, v184
	v_mov_b32_e32 v184, v179
	s_nop 1
	v_permlane32_swap_b32_e32 v184, v179
	s_waitcnt lgkmcnt(0)
	v_add_f32_e32 v179, v179, v184
	v_fmac_f32_e32 v181, v179, v238
	v_mul_f32_e32 v66, v66, v181
	v_cvt_pk_bf16_f32 v179, v183, s0
	v_cvt_pk_bf16_f32 v66, v66, s0
	global_store_short v[62:63], v179, off
	global_store_short v[62:63], v66, off offset:512
	v_lshlrev_b32_e32 v62, 16, v177
	v_add_f32_e32 v62, v62, v237
	v_mul_f32_e32 v63, v62, v62
	s_nop 1
	v_mov_b32_dpp v63, v63 quad_perm:[1,0,3,2] row_mask:0xf bank_mask:0xf
	s_waitcnt lgkmcnt(0)
	v_fmac_f32_e32 v63, v62, v62
	s_nop 1
	v_mov_b32_dpp v66, v63 quad_perm:[2,3,0,1] row_mask:0xf bank_mask:0xf
	s_waitcnt lgkmcnt(0)
	v_add_f32_e32 v63, v63, v66
	s_nop 1
	v_mov_b32_dpp v66, v63 row_half_mirror row_mask:0xf bank_mask:0xf
	s_waitcnt lgkmcnt(0)
	v_add_f32_e32 v63, v63, v66
	s_nop 1
	v_mov_b32_dpp v66, v63 row_mirror row_mask:0xf bank_mask:0xf
	s_waitcnt lgkmcnt(0)
	v_add_f32_e32 v63, v63, v66
	v_mov_b32_e32 v66, v63
	s_nop 1
	v_permlane16_swap_b32_e32 v66, v63
	s_waitcnt lgkmcnt(0)
	v_add_f32_e32 v63, v63, v66
	v_mov_b32_e32 v66, v63
	s_nop 1
	v_permlane32_swap_b32_e32 v66, v63
	s_waitcnt lgkmcnt(0)
	v_add_f32_e32 v63, v63, v66
	v_fmamk_f32 v63, v63, 0x3c800000, v165
	v_rsq_f32_e32 v63, v63
	s_nop 0
	v_mul_f32_e32 v62, v62, v63
	v_lshlrev_b32_e32 v63, 16, v178
	v_mul_f32_e32 v66, 0xbfb8aa3b, v63
	v_exp_f32_e32 v66, v66
	v_mul_f32_e32 v62, v176, v62
	v_add_f32_e32 v66, 1.0, v66
	v_rcp_f32_e32 v66, v66
	s_nop 0
	v_mul_f32_e32 v63, v66, v63
	v_mul_f32_e32 v62, v63, v62
	v_lshlrev_b32_e32 v63, 16, v162
	v_add_f32_e32 v63, v63, v236
	s_nop 1
	v_mov_b32_dpp v66, v63 quad_perm:[1,0,3,2] row_mask:0xf bank_mask:0xf
	v_cvt_pk_bf16_f32 v62, v62, s0
	global_store_short v[58:59], v62, off
	s_waitcnt lgkmcnt(0)
	v_add_f32_e32 v66, v63, v66
	s_nop 1
	v_mov_b32_dpp v162, v66 quad_perm:[2,3,0,1] row_mask:0xf bank_mask:0xf
	s_waitcnt lgkmcnt(0)
	v_add_f32_e32 v66, v66, v162
	s_nop 1
	v_mov_b32_dpp v162, v66 row_half_mirror row_mask:0xf bank_mask:0xf
	s_waitcnt lgkmcnt(0)
	v_add_f32_e32 v66, v66, v162
	s_nop 1
	v_mov_b32_dpp v162, v66 row_mirror row_mask:0xf bank_mask:0xf
	s_waitcnt lgkmcnt(0)
	v_add_f32_e32 v66, v66, v162
	v_mov_b32_e32 v162, v66
	s_nop 1
	v_permlane16_swap_b32_e32 v162, v66
	s_waitcnt lgkmcnt(0)
	v_add_f32_e32 v66, v66, v162
	v_mov_b32_e32 v162, v66
	s_nop 1
	v_permlane32_swap_b32_e32 v162, v66
	s_waitcnt lgkmcnt(0)
	v_add_f32_e32 v66, v66, v162
	v_fmac_f32_e32 v63, 0xbc800000, v66
	v_mul_f32_e32 v66, v63, v63
	s_nop 1
	v_mov_b32_dpp v66, v66 quad_perm:[1,0,3,2] row_mask:0xf bank_mask:0xf
	s_waitcnt lgkmcnt(0)
	v_fmac_f32_e32 v66, v63, v63
	s_nop 1
	v_mov_b32_dpp v162, v66 quad_perm:[2,3,0,1] row_mask:0xf bank_mask:0xf
	s_waitcnt lgkmcnt(0)
	v_add_f32_e32 v66, v66, v162
	s_nop 1
	v_mov_b32_dpp v162, v66 row_half_mirror row_mask:0xf bank_mask:0xf
	s_waitcnt lgkmcnt(0)
	v_add_f32_e32 v66, v66, v162
	s_nop 1
	v_mov_b32_dpp v162, v66 row_mirror row_mask:0xf bank_mask:0xf
	s_waitcnt lgkmcnt(0)
	v_add_f32_e32 v66, v66, v162
	v_mov_b32_e32 v162, v66
	s_nop 1
	v_permlane16_swap_b32_e32 v162, v66
	s_waitcnt lgkmcnt(0)
	v_add_f32_e32 v66, v66, v162
	v_mov_b32_e32 v162, v66
	s_nop 1
	v_permlane32_swap_b32_e32 v162, v66
	s_waitcnt lgkmcnt(0)
	v_add_f32_e32 v66, v66, v162
	v_fmamk_f32 v66, v66, 0x3c800000, v164
	v_rsq_f32_e32 v66, v66
	s_nop 0
	v_mul_f32_e32 v63, v63, v66
	v_lshlrev_b32_e32 v66, 16, v161
	v_mul_f32_e32 v66, v235, v66
	v_mul_f32_e32 v161, v66, v172
	s_nop 1
	v_mov_b32_dpp v161, v161 quad_perm:[1,0,3,2] row_mask:0xf bank_mask:0xf
	v_fma_f32 v63, v173, v63, v170
	s_waitcnt lgkmcnt(0)
	v_fmac_f32_e32 v161, v66, v172
	s_nop 1
	v_mov_b32_dpp v66, v161 quad_perm:[2,3,0,1] row_mask:0xf bank_mask:0xf
	s_waitcnt lgkmcnt(0)
	v_add_f32_e32 v66, v161, v66
	s_nop 1
	v_mov_b32_dpp v161, v66 row_half_mirror row_mask:0xf bank_mask:0xf
	s_waitcnt lgkmcnt(0)
	v_add_f32_e32 v66, v66, v161
	s_nop 1
	v_mov_b32_dpp v161, v66 row_mirror row_mask:0xf bank_mask:0xf
	s_waitcnt lgkmcnt(0)
	v_add_f32_e32 v66, v66, v161
	v_mov_b32_e32 v161, v66
	s_nop 1
	v_permlane16_swap_b32_e32 v161, v66
	s_waitcnt lgkmcnt(0)
	v_add_f32_e32 v66, v66, v161
	v_mov_b32_e32 v161, v66
	s_nop 1
	v_permlane32_swap_b32_e32 v161, v66
	s_waitcnt lgkmcnt(0)
	v_add_f32_e32 v66, v66, v161
	v_fmac_f32_e32 v63, v66, v234
	v_mul_f32_e32 v63, v67, v63
	v_cvt_pk_bf16_f32 v62, v63, s0
	global_store_short v[58:59], v62, off offset:512
	v_lshlrev_b32_e32 v58, 16, v159
	v_add_f32_e32 v58, v58, v233
	v_mul_f32_e32 v59, v58, v58
	s_nop 1
	v_mov_b32_dpp v59, v59 quad_perm:[1,0,3,2] row_mask:0xf bank_mask:0xf
	s_waitcnt lgkmcnt(0)
	v_fmac_f32_e32 v59, v58, v58
	s_nop 1
	v_mov_b32_dpp v62, v59 quad_perm:[2,3,0,1] row_mask:0xf bank_mask:0xf
	s_waitcnt lgkmcnt(0)
	v_add_f32_e32 v59, v59, v62
	s_nop 1
	v_mov_b32_dpp v62, v59 row_half_mirror row_mask:0xf bank_mask:0xf
	s_waitcnt lgkmcnt(0)
	v_add_f32_e32 v59, v59, v62
	s_nop 1
	v_mov_b32_dpp v62, v59 row_mirror row_mask:0xf bank_mask:0xf
	s_waitcnt lgkmcnt(0)
	v_add_f32_e32 v59, v59, v62
	v_mov_b32_e32 v62, v59
	s_nop 1
	v_permlane16_swap_b32_e32 v62, v59
	s_waitcnt lgkmcnt(0)
	v_add_f32_e32 v59, v59, v62
	v_mov_b32_e32 v62, v59
	s_nop 1
	v_permlane32_swap_b32_e32 v62, v59
	s_waitcnt lgkmcnt(0)
	v_add_f32_e32 v59, v59, v62
	v_fmamk_f32 v59, v59, 0x3c800000, v165
	v_rsq_f32_e32 v59, v59
	s_nop 0
	v_mul_f32_e32 v58, v58, v59
	v_lshlrev_b32_e32 v59, 16, v160
	v_mul_f32_e32 v62, 0xbfb8aa3b, v59
	v_exp_f32_e32 v62, v62
	v_mul_f32_e32 v58, v176, v58
	v_add_f32_e32 v62, 1.0, v62
	v_rcp_f32_e32 v62, v62
	s_nop 0
	v_mul_f32_e32 v59, v62, v59
	v_mul_f32_e32 v58, v59, v58
	v_lshlrev_b32_e32 v59, 16, v158
	v_add_f32_e32 v59, v59, v232
	s_nop 1
	v_mov_b32_dpp v62, v59 quad_perm:[1,0,3,2] row_mask:0xf bank_mask:0xf
	v_cvt_pk_bf16_f32 v58, v58, s0
	global_store_short v[56:57], v58, off
	s_waitcnt lgkmcnt(0)
	v_add_f32_e32 v62, v59, v62
	s_nop 1
	v_mov_b32_dpp v63, v62 quad_perm:[2,3,0,1] row_mask:0xf bank_mask:0xf
	s_waitcnt lgkmcnt(0)
	v_add_f32_e32 v62, v62, v63
	s_nop 1
	v_mov_b32_dpp v63, v62 row_half_mirror row_mask:0xf bank_mask:0xf
	s_waitcnt lgkmcnt(0)
	v_add_f32_e32 v62, v62, v63
	s_nop 1
	v_mov_b32_dpp v63, v62 row_mirror row_mask:0xf bank_mask:0xf
	s_waitcnt lgkmcnt(0)
	v_add_f32_e32 v62, v62, v63
	v_mov_b32_e32 v63, v62
	s_nop 1
	v_permlane16_swap_b32_e32 v63, v62
	s_waitcnt lgkmcnt(0)
	v_add_f32_e32 v62, v62, v63
	v_mov_b32_e32 v63, v62
	s_nop 1
	v_permlane32_swap_b32_e32 v63, v62
	s_waitcnt lgkmcnt(0)
	v_add_f32_e32 v62, v62, v63
	v_fmac_f32_e32 v59, 0xbc800000, v62
	v_mul_f32_e32 v62, v59, v59
	s_nop 1
	v_mov_b32_dpp v62, v62 quad_perm:[1,0,3,2] row_mask:0xf bank_mask:0xf
	s_waitcnt lgkmcnt(0)
	v_fmac_f32_e32 v62, v59, v59
	s_nop 1
	v_mov_b32_dpp v63, v62 quad_perm:[2,3,0,1] row_mask:0xf bank_mask:0xf
	s_waitcnt lgkmcnt(0)
	v_add_f32_e32 v62, v62, v63
	s_nop 1
	v_mov_b32_dpp v63, v62 row_half_mirror row_mask:0xf bank_mask:0xf
	s_waitcnt lgkmcnt(0)
	v_add_f32_e32 v62, v62, v63
	s_nop 1
	v_mov_b32_dpp v63, v62 row_mirror row_mask:0xf bank_mask:0xf
	s_waitcnt lgkmcnt(0)
	v_add_f32_e32 v62, v62, v63
	v_mov_b32_e32 v63, v62
	s_nop 1
	v_permlane16_swap_b32_e32 v63, v62
	s_waitcnt lgkmcnt(0)
	v_add_f32_e32 v62, v62, v63
	v_mov_b32_e32 v63, v62
	s_nop 1
	v_permlane32_swap_b32_e32 v63, v62
	s_waitcnt lgkmcnt(0)
	v_add_f32_e32 v62, v62, v63
	v_fmamk_f32 v62, v62, 0x3c800000, v164
	v_rsq_f32_e32 v62, v62
	s_nop 0
	v_mul_f32_e32 v59, v59, v62
	v_lshlrev_b32_e32 v62, 16, v157
	v_mul_f32_e32 v62, v231, v62
	v_mul_f32_e32 v63, v62, v172
	s_nop 1
	v_mov_b32_dpp v63, v63 quad_perm:[1,0,3,2] row_mask:0xf bank_mask:0xf
	v_fma_f32 v59, v173, v59, v170
	s_waitcnt lgkmcnt(0)
	v_fmac_f32_e32 v63, v62, v172
	s_nop 1
	v_mov_b32_dpp v62, v63 quad_perm:[2,3,0,1] row_mask:0xf bank_mask:0xf
	s_waitcnt lgkmcnt(0)
	v_add_f32_e32 v62, v63, v62
	s_nop 1
	v_mov_b32_dpp v63, v62 row_half_mirror row_mask:0xf bank_mask:0xf
	s_waitcnt lgkmcnt(0)
	v_add_f32_e32 v62, v62, v63
	s_nop 1
	v_mov_b32_dpp v63, v62 row_mirror row_mask:0xf bank_mask:0xf
	s_waitcnt lgkmcnt(0)
	v_add_f32_e32 v62, v62, v63
	v_mov_b32_e32 v63, v62
	s_nop 1
	v_permlane16_swap_b32_e32 v63, v62
	s_waitcnt lgkmcnt(0)
	v_add_f32_e32 v62, v62, v63
	v_mov_b32_e32 v63, v62
	s_nop 1
	v_permlane32_swap_b32_e32 v63, v62
	s_waitcnt lgkmcnt(0)
	v_add_f32_e32 v62, v62, v63
	v_fmac_f32_e32 v59, v62, v230
	v_mul_f32_e32 v59, v64, v59
	v_cvt_pk_bf16_f32 v58, v59, s0
	global_store_short v[56:57], v58, off offset:512
	v_lshlrev_b32_e32 v56, 16, v155
	v_add_f32_e32 v56, v56, v229
	v_mul_f32_e32 v57, v56, v56
	s_nop 1
	v_mov_b32_dpp v57, v57 quad_perm:[1,0,3,2] row_mask:0xf bank_mask:0xf
	s_waitcnt lgkmcnt(0)
	v_fmac_f32_e32 v57, v56, v56
	s_nop 1
	v_mov_b32_dpp v58, v57 quad_perm:[2,3,0,1] row_mask:0xf bank_mask:0xf
	s_waitcnt lgkmcnt(0)
	v_add_f32_e32 v57, v57, v58
	s_nop 1
	v_mov_b32_dpp v58, v57 row_half_mirror row_mask:0xf bank_mask:0xf
	s_waitcnt lgkmcnt(0)
	v_add_f32_e32 v57, v57, v58
	s_nop 1
	v_mov_b32_dpp v58, v57 row_mirror row_mask:0xf bank_mask:0xf
	s_waitcnt lgkmcnt(0)
	v_add_f32_e32 v57, v57, v58
	v_mov_b32_e32 v58, v57
	s_nop 1
	v_permlane16_swap_b32_e32 v58, v57
	s_waitcnt lgkmcnt(0)
	v_add_f32_e32 v57, v57, v58
	v_mov_b32_e32 v58, v57
	s_nop 1
	v_permlane32_swap_b32_e32 v58, v57
	s_waitcnt lgkmcnt(0)
	v_add_f32_e32 v57, v57, v58
	v_fmamk_f32 v57, v57, 0x3c800000, v165
	v_rsq_f32_e32 v57, v57
	s_nop 0
	v_mul_f32_e32 v56, v56, v57
	v_lshlrev_b32_e32 v57, 16, v156
	v_mul_f32_e32 v58, 0xbfb8aa3b, v57
	v_exp_f32_e32 v58, v58
	v_mul_f32_e32 v56, v176, v56
	v_add_f32_e32 v58, 1.0, v58
	v_rcp_f32_e32 v58, v58
	s_nop 0
	v_mul_f32_e32 v57, v58, v57
	v_mul_f32_e32 v56, v57, v56
	v_lshlrev_b32_e32 v57, 16, v154
	v_add_f32_e32 v57, v57, v228
	s_nop 1
	v_mov_b32_dpp v58, v57 quad_perm:[1,0,3,2] row_mask:0xf bank_mask:0xf
	v_cvt_pk_bf16_f32 v56, v56, s0
	global_store_short v[52:53], v56, off
	s_waitcnt lgkmcnt(0)
	v_add_f32_e32 v58, v57, v58
	s_nop 1
	v_mov_b32_dpp v59, v58 quad_perm:[2,3,0,1] row_mask:0xf bank_mask:0xf
	s_waitcnt lgkmcnt(0)
	v_add_f32_e32 v58, v58, v59
	s_nop 1
	v_mov_b32_dpp v59, v58 row_half_mirror row_mask:0xf bank_mask:0xf
	s_waitcnt lgkmcnt(0)
	v_add_f32_e32 v58, v58, v59
	s_nop 1
	v_mov_b32_dpp v59, v58 row_mirror row_mask:0xf bank_mask:0xf
	s_waitcnt lgkmcnt(0)
	v_add_f32_e32 v58, v58, v59
	v_mov_b32_e32 v59, v58
	s_nop 1
	v_permlane16_swap_b32_e32 v59, v58
	s_waitcnt lgkmcnt(0)
	v_add_f32_e32 v58, v58, v59
	v_mov_b32_e32 v59, v58
	s_nop 1
	v_permlane32_swap_b32_e32 v59, v58
	s_waitcnt lgkmcnt(0)
	v_add_f32_e32 v58, v58, v59
	v_fmac_f32_e32 v57, 0xbc800000, v58
	v_mul_f32_e32 v58, v57, v57
	s_nop 1
	v_mov_b32_dpp v58, v58 quad_perm:[1,0,3,2] row_mask:0xf bank_mask:0xf
	s_waitcnt lgkmcnt(0)
	v_fmac_f32_e32 v58, v57, v57
	s_nop 1
	v_mov_b32_dpp v59, v58 quad_perm:[2,3,0,1] row_mask:0xf bank_mask:0xf
	s_waitcnt lgkmcnt(0)
	v_add_f32_e32 v58, v58, v59
	s_nop 1
	v_mov_b32_dpp v59, v58 row_half_mirror row_mask:0xf bank_mask:0xf
	s_waitcnt lgkmcnt(0)
	v_add_f32_e32 v58, v58, v59
	s_nop 1
	v_mov_b32_dpp v59, v58 row_mirror row_mask:0xf bank_mask:0xf
	s_waitcnt lgkmcnt(0)
	v_add_f32_e32 v58, v58, v59
	v_mov_b32_e32 v59, v58
	s_nop 1
	v_permlane16_swap_b32_e32 v59, v58
	s_waitcnt lgkmcnt(0)
	v_add_f32_e32 v58, v58, v59
	v_mov_b32_e32 v59, v58
	s_nop 1
	v_permlane32_swap_b32_e32 v59, v58
	s_waitcnt lgkmcnt(0)
	v_add_f32_e32 v58, v58, v59
	v_fmamk_f32 v58, v58, 0x3c800000, v164
	v_rsq_f32_e32 v58, v58
	s_nop 0
	v_mul_f32_e32 v57, v57, v58
	v_lshlrev_b32_e32 v58, 16, v153
	v_mul_f32_e32 v58, v227, v58
	v_mul_f32_e32 v59, v58, v172
	s_nop 1
	v_mov_b32_dpp v59, v59 quad_perm:[1,0,3,2] row_mask:0xf bank_mask:0xf
	v_fma_f32 v57, v173, v57, v170
	s_waitcnt lgkmcnt(0)
	v_fmac_f32_e32 v59, v58, v172
	s_nop 1
	v_mov_b32_dpp v58, v59 quad_perm:[2,3,0,1] row_mask:0xf bank_mask:0xf
	s_waitcnt lgkmcnt(0)
	v_add_f32_e32 v58, v59, v58
	s_nop 1
	v_mov_b32_dpp v59, v58 row_half_mirror row_mask:0xf bank_mask:0xf
	s_waitcnt lgkmcnt(0)
	v_add_f32_e32 v58, v58, v59
	s_nop 1
	v_mov_b32_dpp v59, v58 row_mirror row_mask:0xf bank_mask:0xf
	s_waitcnt lgkmcnt(0)
	v_add_f32_e32 v58, v58, v59
	v_mov_b32_e32 v59, v58
	s_nop 1
	v_permlane16_swap_b32_e32 v59, v58
	s_waitcnt lgkmcnt(0)
	v_add_f32_e32 v58, v58, v59
	v_mov_b32_e32 v59, v58
	s_nop 1
	v_permlane32_swap_b32_e32 v59, v58
	s_waitcnt lgkmcnt(0)
	v_add_f32_e32 v58, v58, v59
	v_fmac_f32_e32 v57, v58, v226
	v_mul_f32_e32 v57, v65, v57
	v_cvt_pk_bf16_f32 v56, v57, s0
	global_store_short v[52:53], v56, off offset:512
	v_lshlrev_b32_e32 v52, 16, v151
	v_add_f32_e32 v52, v52, v225
	v_mul_f32_e32 v53, v52, v52
	s_nop 1
	v_mov_b32_dpp v53, v53 quad_perm:[1,0,3,2] row_mask:0xf bank_mask:0xf
	s_waitcnt lgkmcnt(0)
	v_fmac_f32_e32 v53, v52, v52
	s_nop 1
	v_mov_b32_dpp v56, v53 quad_perm:[2,3,0,1] row_mask:0xf bank_mask:0xf
	s_waitcnt lgkmcnt(0)
	v_add_f32_e32 v53, v53, v56
	s_nop 1
	v_mov_b32_dpp v56, v53 row_half_mirror row_mask:0xf bank_mask:0xf
	s_waitcnt lgkmcnt(0)
	v_add_f32_e32 v53, v53, v56
	s_nop 1
	v_mov_b32_dpp v56, v53 row_mirror row_mask:0xf bank_mask:0xf
	s_waitcnt lgkmcnt(0)
	v_add_f32_e32 v53, v53, v56
	v_mov_b32_e32 v56, v53
	s_nop 1
	v_permlane16_swap_b32_e32 v56, v53
	s_waitcnt lgkmcnt(0)
	v_add_f32_e32 v53, v53, v56
	v_mov_b32_e32 v56, v53
	s_nop 1
	v_permlane32_swap_b32_e32 v56, v53
	s_waitcnt lgkmcnt(0)
	v_add_f32_e32 v53, v53, v56
	v_fmamk_f32 v53, v53, 0x3c800000, v165
	v_rsq_f32_e32 v53, v53
	s_nop 0
	v_mul_f32_e32 v52, v52, v53
	v_lshlrev_b32_e32 v53, 16, v152
	v_mul_f32_e32 v56, 0xbfb8aa3b, v53
	v_exp_f32_e32 v56, v56
	v_mul_f32_e32 v52, v176, v52
	v_add_f32_e32 v56, 1.0, v56
	v_rcp_f32_e32 v56, v56
	s_nop 0
	v_mul_f32_e32 v53, v56, v53
	v_mul_f32_e32 v52, v53, v52
	v_lshlrev_b32_e32 v53, 16, v150
	v_add_f32_e32 v53, v53, v224
	s_nop 1
	v_mov_b32_dpp v56, v53 quad_perm:[1,0,3,2] row_mask:0xf bank_mask:0xf
	v_cvt_pk_bf16_f32 v52, v52, s0
	global_store_short v[50:51], v52, off
	s_waitcnt lgkmcnt(0)
	v_add_f32_e32 v56, v53, v56
	s_nop 1
	v_mov_b32_dpp v57, v56 quad_perm:[2,3,0,1] row_mask:0xf bank_mask:0xf
	s_waitcnt lgkmcnt(0)
	v_add_f32_e32 v56, v56, v57
	s_nop 1
	v_mov_b32_dpp v57, v56 row_half_mirror row_mask:0xf bank_mask:0xf
	s_waitcnt lgkmcnt(0)
	v_add_f32_e32 v56, v56, v57
	s_nop 1
	v_mov_b32_dpp v57, v56 row_mirror row_mask:0xf bank_mask:0xf
	s_waitcnt lgkmcnt(0)
	v_add_f32_e32 v56, v56, v57
	v_mov_b32_e32 v57, v56
	s_nop 1
	v_permlane16_swap_b32_e32 v57, v56
	s_waitcnt lgkmcnt(0)
	v_add_f32_e32 v56, v56, v57
	v_mov_b32_e32 v57, v56
	s_nop 1
	v_permlane32_swap_b32_e32 v57, v56
	s_waitcnt lgkmcnt(0)
	v_add_f32_e32 v56, v56, v57
	v_fmac_f32_e32 v53, 0xbc800000, v56
	v_mul_f32_e32 v56, v53, v53
	s_nop 1
	v_mov_b32_dpp v56, v56 quad_perm:[1,0,3,2] row_mask:0xf bank_mask:0xf
	s_waitcnt lgkmcnt(0)
	v_fmac_f32_e32 v56, v53, v53
	s_nop 1
	v_mov_b32_dpp v57, v56 quad_perm:[2,3,0,1] row_mask:0xf bank_mask:0xf
	s_waitcnt lgkmcnt(0)
	v_add_f32_e32 v56, v56, v57
	s_nop 1
	v_mov_b32_dpp v57, v56 row_half_mirror row_mask:0xf bank_mask:0xf
	s_waitcnt lgkmcnt(0)
	v_add_f32_e32 v56, v56, v57
	s_nop 1
	v_mov_b32_dpp v57, v56 row_mirror row_mask:0xf bank_mask:0xf
	s_waitcnt lgkmcnt(0)
	v_add_f32_e32 v56, v56, v57
	v_mov_b32_e32 v57, v56
	s_nop 1
	v_permlane16_swap_b32_e32 v57, v56
	s_waitcnt lgkmcnt(0)
	v_add_f32_e32 v56, v56, v57
	v_mov_b32_e32 v57, v56
	s_nop 1
	v_permlane32_swap_b32_e32 v57, v56
	s_waitcnt lgkmcnt(0)
	v_add_f32_e32 v56, v56, v57
	v_fmamk_f32 v56, v56, 0x3c800000, v164
	v_rsq_f32_e32 v56, v56
	s_nop 0
	v_mul_f32_e32 v53, v53, v56
	v_lshlrev_b32_e32 v56, 16, v149
	v_mul_f32_e32 v56, v191, v56
	v_mul_f32_e32 v57, v56, v172
	s_nop 1
	v_mov_b32_dpp v57, v57 quad_perm:[1,0,3,2] row_mask:0xf bank_mask:0xf
	v_fma_f32 v53, v173, v53, v170
	s_waitcnt lgkmcnt(0)
	v_fmac_f32_e32 v57, v56, v172
	s_nop 1
	v_mov_b32_dpp v56, v57 quad_perm:[2,3,0,1] row_mask:0xf bank_mask:0xf
	s_waitcnt lgkmcnt(0)
	v_add_f32_e32 v56, v57, v56
	s_nop 1
	v_mov_b32_dpp v57, v56 row_half_mirror row_mask:0xf bank_mask:0xf
	s_waitcnt lgkmcnt(0)
	v_add_f32_e32 v56, v56, v57
	s_nop 1
	v_mov_b32_dpp v57, v56 row_mirror row_mask:0xf bank_mask:0xf
	s_waitcnt lgkmcnt(0)
	v_add_f32_e32 v56, v56, v57
	v_mov_b32_e32 v57, v56
	s_nop 1
	v_permlane16_swap_b32_e32 v57, v56
	s_waitcnt lgkmcnt(0)
	v_add_f32_e32 v56, v56, v57
	v_mov_b32_e32 v57, v56
	s_nop 1
	v_permlane32_swap_b32_e32 v57, v56
	s_waitcnt lgkmcnt(0)
	v_add_f32_e32 v56, v56, v57
	v_fmac_f32_e32 v53, v56, v190
	v_mul_f32_e32 v53, v60, v53
	v_cvt_pk_bf16_f32 v52, v53, s0
	global_store_short v[50:51], v52, off offset:512
	v_lshlrev_b32_e32 v50, 16, v147
	v_add_f32_e32 v50, v50, v189
	v_mul_f32_e32 v51, v50, v50
	s_nop 1
	v_mov_b32_dpp v51, v51 quad_perm:[1,0,3,2] row_mask:0xf bank_mask:0xf
	s_waitcnt lgkmcnt(0)
	v_fmac_f32_e32 v51, v50, v50
	s_nop 1
	v_mov_b32_dpp v52, v51 quad_perm:[2,3,0,1] row_mask:0xf bank_mask:0xf
	s_waitcnt lgkmcnt(0)
	v_add_f32_e32 v51, v51, v52
	s_nop 1
	v_mov_b32_dpp v52, v51 row_half_mirror row_mask:0xf bank_mask:0xf
	s_waitcnt lgkmcnt(0)
	v_add_f32_e32 v51, v51, v52
	s_nop 1
	v_mov_b32_dpp v52, v51 row_mirror row_mask:0xf bank_mask:0xf
	s_waitcnt lgkmcnt(0)
	v_add_f32_e32 v51, v51, v52
	v_mov_b32_e32 v52, v51
	s_nop 1
	v_permlane16_swap_b32_e32 v52, v51
	s_waitcnt lgkmcnt(0)
	v_add_f32_e32 v51, v51, v52
	v_mov_b32_e32 v52, v51
	s_nop 1
	v_permlane32_swap_b32_e32 v52, v51
	s_waitcnt lgkmcnt(0)
	v_add_f32_e32 v51, v51, v52
	v_fmamk_f32 v51, v51, 0x3c800000, v165
	v_rsq_f32_e32 v51, v51
	s_nop 0
	v_mul_f32_e32 v50, v50, v51
	v_lshlrev_b32_e32 v51, 16, v148
	v_mul_f32_e32 v52, 0xbfb8aa3b, v51
	v_exp_f32_e32 v52, v52
	v_mul_f32_e32 v50, v176, v50
	v_add_f32_e32 v52, 1.0, v52
	v_rcp_f32_e32 v52, v52
	s_nop 0
	v_mul_f32_e32 v51, v52, v51
	v_mul_f32_e32 v50, v51, v50
	v_lshlrev_b32_e32 v51, 16, v146
	v_add_f32_e32 v51, v51, v188
	s_nop 1
	v_mov_b32_dpp v52, v51 quad_perm:[1,0,3,2] row_mask:0xf bank_mask:0xf
	v_cvt_pk_bf16_f32 v50, v50, s0
	global_store_short v[48:49], v50, off
	s_waitcnt lgkmcnt(0)
	v_add_f32_e32 v52, v51, v52
	s_nop 1
	v_mov_b32_dpp v53, v52 quad_perm:[2,3,0,1] row_mask:0xf bank_mask:0xf
	s_waitcnt lgkmcnt(0)
	v_add_f32_e32 v52, v52, v53
	s_nop 1
	v_mov_b32_dpp v53, v52 row_half_mirror row_mask:0xf bank_mask:0xf
	s_waitcnt lgkmcnt(0)
	v_add_f32_e32 v52, v52, v53
	s_nop 1
	v_mov_b32_dpp v53, v52 row_mirror row_mask:0xf bank_mask:0xf
	s_waitcnt lgkmcnt(0)
	v_add_f32_e32 v52, v52, v53
	v_mov_b32_e32 v53, v52
	s_nop 1
	v_permlane16_swap_b32_e32 v53, v52
	s_waitcnt lgkmcnt(0)
	v_add_f32_e32 v52, v52, v53
	v_mov_b32_e32 v53, v52
	s_nop 1
	v_permlane32_swap_b32_e32 v53, v52
	s_waitcnt lgkmcnt(0)
	v_add_f32_e32 v52, v52, v53
	v_fmac_f32_e32 v51, 0xbc800000, v52
	v_mul_f32_e32 v52, v51, v51
	s_nop 1
	v_mov_b32_dpp v52, v52 quad_perm:[1,0,3,2] row_mask:0xf bank_mask:0xf
	s_waitcnt lgkmcnt(0)
	v_fmac_f32_e32 v52, v51, v51
	s_nop 1
	v_mov_b32_dpp v53, v52 quad_perm:[2,3,0,1] row_mask:0xf bank_mask:0xf
	s_waitcnt lgkmcnt(0)
	v_add_f32_e32 v52, v52, v53
	s_nop 1
	v_mov_b32_dpp v53, v52 row_half_mirror row_mask:0xf bank_mask:0xf
	s_waitcnt lgkmcnt(0)
	v_add_f32_e32 v52, v52, v53
	s_nop 1
	v_mov_b32_dpp v53, v52 row_mirror row_mask:0xf bank_mask:0xf
	s_waitcnt lgkmcnt(0)
	v_add_f32_e32 v52, v52, v53
	v_mov_b32_e32 v53, v52
	s_nop 1
	v_permlane16_swap_b32_e32 v53, v52
	s_waitcnt lgkmcnt(0)
	v_add_f32_e32 v52, v52, v53
	v_mov_b32_e32 v53, v52
	s_nop 1
	v_permlane32_swap_b32_e32 v53, v52
	s_waitcnt lgkmcnt(0)
	v_add_f32_e32 v52, v52, v53
	v_fmamk_f32 v52, v52, 0x3c800000, v164
	v_rsq_f32_e32 v52, v52
	s_nop 0
	v_mul_f32_e32 v51, v51, v52
	v_lshlrev_b32_e32 v52, 16, v145
	v_mul_f32_e32 v52, v187, v52
	v_mul_f32_e32 v53, v52, v172
	s_nop 1
	v_mov_b32_dpp v53, v53 quad_perm:[1,0,3,2] row_mask:0xf bank_mask:0xf
	v_fma_f32 v51, v173, v51, v170
	s_waitcnt lgkmcnt(0)
	v_fmac_f32_e32 v53, v52, v172
	s_nop 1
	v_mov_b32_dpp v52, v53 quad_perm:[2,3,0,1] row_mask:0xf bank_mask:0xf
	s_waitcnt lgkmcnt(0)
	v_add_f32_e32 v52, v53, v52
	s_nop 1
	v_mov_b32_dpp v53, v52 row_half_mirror row_mask:0xf bank_mask:0xf
	s_waitcnt lgkmcnt(0)
	v_add_f32_e32 v52, v52, v53
	s_nop 1
	v_mov_b32_dpp v53, v52 row_mirror row_mask:0xf bank_mask:0xf
	s_waitcnt lgkmcnt(0)
	v_add_f32_e32 v52, v52, v53
	v_mov_b32_e32 v53, v52
	s_nop 1
	v_permlane16_swap_b32_e32 v53, v52
	s_waitcnt lgkmcnt(0)
	v_add_f32_e32 v52, v52, v53
	v_mov_b32_e32 v53, v52
	s_nop 1
	v_permlane32_swap_b32_e32 v53, v52
	s_waitcnt lgkmcnt(0)
	v_add_f32_e32 v52, v52, v53
	v_fmac_f32_e32 v51, v52, v186
	v_mul_f32_e32 v51, v61, v51
	v_cvt_pk_bf16_f32 v50, v51, s0
	global_store_short v[48:49], v50, off offset:512
	v_lshlrev_b32_e32 v48, 16, v143
	v_add_f32_e32 v48, v48, v185
	v_mul_f32_e32 v49, v48, v48
	s_nop 1
	v_mov_b32_dpp v49, v49 quad_perm:[1,0,3,2] row_mask:0xf bank_mask:0xf
	s_waitcnt lgkmcnt(0)
	v_fmac_f32_e32 v49, v48, v48
	s_nop 1
	v_mov_b32_dpp v50, v49 quad_perm:[2,3,0,1] row_mask:0xf bank_mask:0xf
	s_waitcnt lgkmcnt(0)
	v_add_f32_e32 v49, v49, v50
	s_nop 1
	v_mov_b32_dpp v50, v49 row_half_mirror row_mask:0xf bank_mask:0xf
	s_waitcnt lgkmcnt(0)
	v_add_f32_e32 v49, v49, v50
	s_nop 1
	v_mov_b32_dpp v50, v49 row_mirror row_mask:0xf bank_mask:0xf
	s_waitcnt lgkmcnt(0)
	v_add_f32_e32 v49, v49, v50
	v_mov_b32_e32 v50, v49
	s_nop 1
	v_permlane16_swap_b32_e32 v50, v49
	s_waitcnt lgkmcnt(0)
	v_add_f32_e32 v49, v49, v50
	v_mov_b32_e32 v50, v49
	s_nop 1
	v_permlane32_swap_b32_e32 v50, v49
	s_waitcnt lgkmcnt(0)
	v_add_f32_e32 v49, v49, v50
	v_fmamk_f32 v49, v49, 0x3c800000, v165
	v_rsq_f32_e32 v49, v49
	s_nop 0
	v_mul_f32_e32 v48, v48, v49
	v_lshlrev_b32_e32 v49, 16, v144
	v_mul_f32_e32 v50, 0xbfb8aa3b, v49
	v_exp_f32_e32 v50, v50
	v_mul_f32_e32 v48, v176, v48
	v_add_f32_e32 v50, 1.0, v50
	v_rcp_f32_e32 v50, v50
	s_nop 0
	v_mul_f32_e32 v49, v50, v49
	v_mul_f32_e32 v48, v49, v48
	v_lshlrev_b32_e32 v49, 16, v142
	v_add_f32_e32 v49, v49, v182
	s_nop 1
	v_mov_b32_dpp v50, v49 quad_perm:[1,0,3,2] row_mask:0xf bank_mask:0xf
	v_cvt_pk_bf16_f32 v48, v48, s0
	global_store_short v[46:47], v48, off
	s_waitcnt lgkmcnt(0)
	v_add_f32_e32 v50, v49, v50
	s_nop 1
	v_mov_b32_dpp v51, v50 quad_perm:[2,3,0,1] row_mask:0xf bank_mask:0xf
	s_waitcnt lgkmcnt(0)
	v_add_f32_e32 v50, v50, v51
	s_nop 1
	v_mov_b32_dpp v51, v50 row_half_mirror row_mask:0xf bank_mask:0xf
	s_waitcnt lgkmcnt(0)
	v_add_f32_e32 v50, v50, v51
	s_nop 1
	v_mov_b32_dpp v51, v50 row_mirror row_mask:0xf bank_mask:0xf
	s_waitcnt lgkmcnt(0)
	v_add_f32_e32 v50, v50, v51
	v_mov_b32_e32 v51, v50
	s_nop 1
	v_permlane16_swap_b32_e32 v51, v50
	s_waitcnt lgkmcnt(0)
	v_add_f32_e32 v50, v50, v51
	v_mov_b32_e32 v51, v50
	s_nop 1
	v_permlane32_swap_b32_e32 v51, v50
	s_waitcnt lgkmcnt(0)
	v_add_f32_e32 v50, v50, v51
	v_fmac_f32_e32 v49, 0xbc800000, v50
	v_mul_f32_e32 v50, v49, v49
	s_nop 1
	v_mov_b32_dpp v50, v50 quad_perm:[1,0,3,2] row_mask:0xf bank_mask:0xf
	s_waitcnt lgkmcnt(0)
	v_fmac_f32_e32 v50, v49, v49
	s_nop 1
	v_mov_b32_dpp v51, v50 quad_perm:[2,3,0,1] row_mask:0xf bank_mask:0xf
	s_waitcnt lgkmcnt(0)
	v_add_f32_e32 v50, v50, v51
	s_nop 1
	v_mov_b32_dpp v51, v50 row_half_mirror row_mask:0xf bank_mask:0xf
	s_waitcnt lgkmcnt(0)
	v_add_f32_e32 v50, v50, v51
	s_nop 1
	v_mov_b32_dpp v51, v50 row_mirror row_mask:0xf bank_mask:0xf
	s_waitcnt lgkmcnt(0)
	v_add_f32_e32 v50, v50, v51
	v_mov_b32_e32 v51, v50
	s_nop 1
	v_permlane16_swap_b32_e32 v51, v50
	s_waitcnt lgkmcnt(0)
	v_add_f32_e32 v50, v50, v51
	v_mov_b32_e32 v51, v50
	s_nop 1
	v_permlane32_swap_b32_e32 v51, v50
	s_waitcnt lgkmcnt(0)
	v_add_f32_e32 v50, v50, v51
	v_fmamk_f32 v50, v50, 0x3c800000, v164
	v_rsq_f32_e32 v50, v50
	s_nop 0
	v_mul_f32_e32 v49, v49, v50
	v_lshlrev_b32_e32 v50, 16, v141
	v_mul_f32_e32 v50, v180, v50
	v_mul_f32_e32 v51, v50, v172
	s_nop 1
	v_mov_b32_dpp v51, v51 quad_perm:[1,0,3,2] row_mask:0xf bank_mask:0xf
	v_fma_f32 v49, v173, v49, v170
	s_waitcnt lgkmcnt(0)
	v_fmac_f32_e32 v51, v50, v172
	s_nop 1
	v_mov_b32_dpp v50, v51 quad_perm:[2,3,0,1] row_mask:0xf bank_mask:0xf
	s_waitcnt lgkmcnt(0)
	v_add_f32_e32 v50, v51, v50
	s_nop 1
	v_mov_b32_dpp v51, v50 row_half_mirror row_mask:0xf bank_mask:0xf
	s_waitcnt lgkmcnt(0)
	v_add_f32_e32 v50, v50, v51
	s_nop 1
	v_mov_b32_dpp v51, v50 row_mirror row_mask:0xf bank_mask:0xf
	s_waitcnt lgkmcnt(0)
	v_add_f32_e32 v50, v50, v51
	v_mov_b32_e32 v51, v50
	s_nop 1
	v_permlane16_swap_b32_e32 v51, v50
	s_waitcnt lgkmcnt(0)
	v_add_f32_e32 v50, v50, v51
	v_mov_b32_e32 v51, v50
	s_nop 1
	v_permlane32_swap_b32_e32 v51, v50
	s_waitcnt lgkmcnt(0)
	v_add_f32_e32 v50, v50, v51
	v_fmac_f32_e32 v49, v50, v175
	v_mul_f32_e32 v49, v54, v49
	v_cvt_pk_bf16_f32 v48, v49, s0
	global_store_short v[46:47], v48, off offset:512
	v_lshlrev_b32_e32 v46, 16, v139
	v_add_f32_e32 v46, v46, v174
	v_mul_f32_e32 v47, v46, v46
	s_nop 1
	v_mov_b32_dpp v47, v47 quad_perm:[1,0,3,2] row_mask:0xf bank_mask:0xf
	s_waitcnt lgkmcnt(0)
	v_fmac_f32_e32 v47, v46, v46
	s_nop 1
	v_mov_b32_dpp v48, v47 quad_perm:[2,3,0,1] row_mask:0xf bank_mask:0xf
	s_waitcnt lgkmcnt(0)
	v_add_f32_e32 v47, v47, v48
	s_nop 1
	v_mov_b32_dpp v48, v47 row_half_mirror row_mask:0xf bank_mask:0xf
	s_waitcnt lgkmcnt(0)
	v_add_f32_e32 v47, v47, v48
	s_nop 1
	v_mov_b32_dpp v48, v47 row_mirror row_mask:0xf bank_mask:0xf
	s_waitcnt lgkmcnt(0)
	v_add_f32_e32 v47, v47, v48
	v_mov_b32_e32 v48, v47
	s_nop 1
	v_permlane16_swap_b32_e32 v48, v47
	s_waitcnt lgkmcnt(0)
	v_add_f32_e32 v47, v47, v48
	v_mov_b32_e32 v48, v47
	s_nop 1
	v_permlane32_swap_b32_e32 v48, v47
	s_waitcnt lgkmcnt(0)
	v_add_f32_e32 v47, v47, v48
	v_fmamk_f32 v47, v47, 0x3c800000, v165
	v_rsq_f32_e32 v47, v47
	s_nop 0
	v_mul_f32_e32 v46, v46, v47
	v_lshlrev_b32_e32 v47, 16, v140
	v_mul_f32_e32 v48, 0xbfb8aa3b, v47
	v_exp_f32_e32 v48, v48
	v_mul_f32_e32 v46, v176, v46
	v_add_f32_e32 v48, 1.0, v48
	v_rcp_f32_e32 v48, v48
	s_nop 0
	v_mul_f32_e32 v47, v48, v47
	v_mul_f32_e32 v46, v47, v46
	v_lshlrev_b32_e32 v47, 16, v138
	v_add_f32_e32 v47, v47, v171
	s_nop 1
	v_mov_b32_dpp v48, v47 quad_perm:[1,0,3,2] row_mask:0xf bank_mask:0xf
	v_cvt_pk_bf16_f32 v46, v46, s0
	global_store_short v[44:45], v46, off
	s_waitcnt lgkmcnt(0)
	v_add_f32_e32 v48, v47, v48
	s_nop 1
	v_mov_b32_dpp v49, v48 quad_perm:[2,3,0,1] row_mask:0xf bank_mask:0xf
	s_waitcnt lgkmcnt(0)
	v_add_f32_e32 v48, v48, v49
	s_nop 1
	v_mov_b32_dpp v49, v48 row_half_mirror row_mask:0xf bank_mask:0xf
	s_waitcnt lgkmcnt(0)
	v_add_f32_e32 v48, v48, v49
	s_nop 1
	v_mov_b32_dpp v49, v48 row_mirror row_mask:0xf bank_mask:0xf
	s_waitcnt lgkmcnt(0)
	v_add_f32_e32 v48, v48, v49
	v_mov_b32_e32 v49, v48
	s_nop 1
	v_permlane16_swap_b32_e32 v49, v48
	s_waitcnt lgkmcnt(0)
	v_add_f32_e32 v48, v48, v49
	v_mov_b32_e32 v49, v48
	s_nop 1
	v_permlane32_swap_b32_e32 v49, v48
	s_waitcnt lgkmcnt(0)
	v_add_f32_e32 v48, v48, v49
	v_fmac_f32_e32 v47, 0xbc800000, v48
	v_mul_f32_e32 v48, v47, v47
	s_nop 1
	v_mov_b32_dpp v48, v48 quad_perm:[1,0,3,2] row_mask:0xf bank_mask:0xf
	s_waitcnt lgkmcnt(0)
	v_fmac_f32_e32 v48, v47, v47
	s_nop 1
	v_mov_b32_dpp v49, v48 quad_perm:[2,3,0,1] row_mask:0xf bank_mask:0xf
	s_waitcnt lgkmcnt(0)
	v_add_f32_e32 v48, v48, v49
	s_nop 1
	v_mov_b32_dpp v49, v48 row_half_mirror row_mask:0xf bank_mask:0xf
	s_waitcnt lgkmcnt(0)
	v_add_f32_e32 v48, v48, v49
	s_nop 1
	v_mov_b32_dpp v49, v48 row_mirror row_mask:0xf bank_mask:0xf
	s_waitcnt lgkmcnt(0)
	v_add_f32_e32 v48, v48, v49
	v_mov_b32_e32 v49, v48
	s_nop 1
	v_permlane16_swap_b32_e32 v49, v48
	s_waitcnt lgkmcnt(0)
	v_add_f32_e32 v48, v48, v49
	v_mov_b32_e32 v49, v48
	s_nop 1
	v_permlane32_swap_b32_e32 v49, v48
	s_waitcnt lgkmcnt(0)
	v_add_f32_e32 v48, v48, v49
	v_fmamk_f32 v48, v48, 0x3c800000, v164
	v_rsq_f32_e32 v48, v48
	s_nop 0
	v_mul_f32_e32 v47, v47, v48
	v_fmac_f32_e32 v170, v173, v47
	v_lshlrev_b32_e32 v47, 16, v137
	v_mul_f32_e32 v47, v169, v47
	v_mul_f32_e32 v48, v47, v172
	s_nop 1
	v_mov_b32_dpp v48, v48 quad_perm:[1,0,3,2] row_mask:0xf bank_mask:0xf
	s_waitcnt lgkmcnt(0)
	v_fmac_f32_e32 v48, v47, v172
	s_nop 1
	v_mov_b32_dpp v47, v48 quad_perm:[2,3,0,1] row_mask:0xf bank_mask:0xf
	s_waitcnt lgkmcnt(0)
	v_add_f32_e32 v47, v48, v47
	s_nop 1
	v_mov_b32_dpp v48, v47 row_half_mirror row_mask:0xf bank_mask:0xf
	s_waitcnt lgkmcnt(0)
	v_add_f32_e32 v47, v47, v48
	s_nop 1
	v_mov_b32_dpp v48, v47 row_mirror row_mask:0xf bank_mask:0xf
	s_waitcnt lgkmcnt(0)
	v_add_f32_e32 v47, v47, v48
	v_mov_b32_e32 v48, v47
	s_nop 1
	v_permlane16_swap_b32_e32 v48, v47
	s_waitcnt lgkmcnt(0)
	v_add_f32_e32 v47, v47, v48
	v_mov_b32_e32 v48, v47
	s_nop 1
	v_permlane32_swap_b32_e32 v48, v47
	s_waitcnt lgkmcnt(0)
	v_add_f32_e32 v47, v47, v48
	v_fmac_f32_e32 v170, v47, v163
	v_mul_f32_e32 v47, v55, v170
	v_cvt_pk_bf16_f32 v46, v47, s0
	global_store_short v[44:45], v46, off offset:512
	global_load_dword v45, v[30:31], off
	s_nop 0
	global_load_dword v44, v[32:33], off
	v_lshlrev_b32_e32 v46, 16, v135
	v_add_f32_e32 v46, v46, v71
	v_lshlrev_b32_e32 v47, 16, v136
	s_waitcnt vmcnt(1)
	v_fmac_f32_e32 v46, v45, v47
	v_mul_f32_e32 v47, 0xbfb8aa3b, v70
	v_exp_f32_e32 v47, v47
	s_nop 0
	v_add_f32_e32 v47, 1.0, v47
	v_rcp_f32_e32 v47, v47
	s_nop 0
	v_mul_f32_e32 v47, v47, v70
	v_mul_f32_e32 v46, v47, v46
	v_mul_f32_e32 v47, v46, v46
	s_nop 1
	v_mov_b32_dpp v47, v47 quad_perm:[1,0,3,2] row_mask:0xf bank_mask:0xf
	s_waitcnt lgkmcnt(0)
	v_fmac_f32_e32 v47, v46, v46
	s_nop 1
	v_mov_b32_dpp v48, v47 quad_perm:[2,3,0,1] row_mask:0xf bank_mask:0xf
	s_waitcnt lgkmcnt(0)
	v_add_f32_e32 v47, v47, v48
	s_nop 1
	v_mov_b32_dpp v48, v47 row_half_mirror row_mask:0xf bank_mask:0xf
	s_waitcnt lgkmcnt(0)
	v_add_f32_e32 v47, v47, v48
	s_nop 1
	v_mov_b32_dpp v48, v47 row_mirror row_mask:0xf bank_mask:0xf
	s_waitcnt lgkmcnt(0)
	v_add_f32_e32 v47, v47, v48
	v_mov_b32_e32 v48, v47
	s_nop 1
	v_permlane16_swap_b32_e32 v48, v47
	s_waitcnt lgkmcnt(0)
	v_add_f32_e32 v47, v47, v48
	v_mov_b32_e32 v48, v47
	s_nop 1
	v_permlane32_swap_b32_e32 v48, v47
	s_and_saveexec_b64 s[0:1], vcc
	s_cbranch_execz .LBB0_1237
	s_waitcnt lgkmcnt(0)
	v_add_f32_e32 v47, v47, v48
	v_mov_b32_e32 v48, s11
	ds_write_b32 v48, v47 offset:4096
